# v12 + sc1 on k1 simi stores
# baseline (speedup 1.0000x reference)
_Z7k1_gemmPKhPf:
	s_load_dwordx4 s[4:7], s[0:1], 0x0
	v_lshrrev_b32_e32 v1, 3, v0
	v_lshlrev_b32_e32 v2, 3, v0
	v_and_b32_e32 v194, 56, v2
	s_movk_i32 s10, 0x600
	s_waitcnt lgkmcnt(0)
	s_add_u32 s0, s4, 0x780000
	s_addc_u32 s1, s5, 0
	s_lshl_b32 s3, s2, 2
	s_lshr_b32 s8, s2, 6
	s_and_b32 s3, s3, 28
	s_add_i32 s8, s3, s8
	s_lshl_b32 s9, s2, 4
	s_add_u32 s2, s4, 0x784000
	s_addc_u32 s3, s5, 0
	s_lshl_b32 s8, s8, 7
	v_or_b32_e32 v4, s8, v1
	v_mov_b64_e32 v[2:3], s[4:5]
	s_and_b32 s9, s9, 0x380
	v_mad_u64_u32 v[2:3], s[10:11], v4, s10, v[2:3]
	v_lshlrev_b32_e32 v226, 1, v194
	v_mov_b32_e32 v227, 0
	v_lshl_add_u64 v[210:211], v[2:3], 0, v[226:227]
	v_or_b32_e32 v2, s9, v1
	v_mul_u32_u24_e32 v2, 0x300, v2
	v_lshlrev_b32_e32 v2, 1, v2
	v_mov_b32_e32 v3, v227
	v_lshl_add_u64 v[2:3], s[4:5], 0, v[2:3]
	v_lshl_add_u64 v[2:3], v[2:3], 0, v[226:227]
	s_mov_b32 s4, 0x600000
	v_add_co_u32_e32 v4, vcc, s4, v2
	s_mov_b32 s4, 0xc000
	s_nop 0
	v_addc_co_u32_e32 v5, vcc, 0, v3, vcc
	v_add_co_u32_e32 v218, vcc, s4, v210
	s_mov_b32 s4, 0x60c000
	s_nop 0
	v_addc_co_u32_e32 v219, vcc, 0, v211, vcc
	v_add_co_u32_e32 v222, vcc, s4, v2
	s_mov_b32 s4, 0x18000
	s_nop 0
	v_addc_co_u32_e32 v223, vcc, 0, v3, vcc
	v_add_co_u32_e32 v228, vcc, s4, v210
	global_load_dwordx4 v[34:37], v[210:211], off
	global_load_dwordx4 v[38:41], v[4:5], off
	v_addc_co_u32_e32 v229, vcc, 0, v211, vcc
	s_mov_b32 s4, 0x618000
	v_add_co_u32_e32 v230, vcc, s4, v2
	global_load_dwordx4 v[42:45], v[218:219], off
	global_load_dwordx4 v[46:49], v[222:223], off
	v_addc_co_u32_e32 v231, vcc, 0, v3, vcc
	s_mov_b32 s4, 0x24000
	v_add_co_u32_e32 v232, vcc, s4, v210
	global_load_dwordx4 v[50:53], v[228:229], off
	global_load_dwordx4 v[54:57], v[230:231], off
	v_addc_co_u32_e32 v233, vcc, 0, v211, vcc
	s_mov_b32 s4, 0x624000
	v_add_co_u32_e32 v234, vcc, s4, v2
	global_load_dwordx4 v[58:61], v[232:233], off
	s_nop 0
	v_addc_co_u32_e32 v235, vcc, 0, v3, vcc
	global_load_dwordx4 v[62:65], v[234:235], off
	s_mov_b64 s[4:5], 0x600000
	v_lshl_add_u64 v[214:215], v[2:3], 0, s[4:5]
	v_lshrrev_b32_e32 v2, 1, v0
	v_and_b32_e32 v226, 31, v0
	v_and_b32_e32 v237, 64, v2
	v_or_b32_e32 v2, v237, v226
	v_mul_u32_u24_e32 v196, 0x48, v2
	global_load_dwordx4 v[66:69], v[210:211], off offset:128
	global_load_dwordx4 v[70:73], v[218:219], off offset:128
	global_load_dwordx4 v[74:77], v[222:223], off offset:128
	global_load_dwordx4 v[78:81], v[228:229], off offset:128
	global_load_dwordx4 v[82:85], v[230:231], off offset:128
	global_load_dwordx4 v[86:89], v[232:233], off offset:128
	global_load_dwordx4 v[90:93], v[234:235], off offset:128
	global_load_dwordx4 v[94:97], v[214:215], off offset:128
	global_load_dwordx4 v[98:101], v[214:215], off offset:256
	global_load_dwordx4 v[102:105], v[210:211], off offset:256
	global_load_dwordx4 v[130:133], v[210:211], off offset:384
	global_load_dwordx4 v[106:109], v[218:219], off offset:256
	global_load_dwordx4 v[134:137], v[218:219], off offset:384
	global_load_dwordx4 v[110:113], v[222:223], off offset:256
	global_load_dwordx4 v[138:141], v[222:223], off offset:384
	global_load_dwordx4 v[114:117], v[228:229], off offset:256
	global_load_dwordx4 v[142:145], v[228:229], off offset:384
	global_load_dwordx4 v[118:121], v[230:231], off offset:256
	global_load_dwordx4 v[146:149], v[230:231], off offset:384
	global_load_dwordx4 v[122:125], v[232:233], off offset:256
	global_load_dwordx4 v[150:153], v[232:233], off offset:384
	global_load_dwordx4 v[126:129], v[234:235], off offset:256
	global_load_dwordx4 v[170:173], v[234:235], off offset:384
	global_load_dwordx4 v[174:177], v[214:215], off offset:384
	global_load_dwordx4 v[154:157], v[214:215], off offset:512
	global_load_dwordx4 v[158:161], v[210:211], off offset:512
	global_load_dwordx4 v[2:5], v[210:211], off offset:640
	global_load_dwordx4 v[6:9], v[214:215], off offset:640
	global_load_dwordx4 v[162:165], v[218:219], off offset:512
	global_load_dwordx4 v[10:13], v[218:219], off offset:640
	global_load_dwordx4 v[166:169], v[222:223], off offset:512
	global_load_dwordx4 v[14:17], v[222:223], off offset:640
	global_load_dwordx4 v[178:181], v[228:229], off offset:512
	global_load_dwordx4 v[18:21], v[228:229], off offset:640
	global_load_dwordx4 v[182:185], v[230:231], off offset:512
	global_load_dwordx4 v[22:25], v[230:231], off offset:640
	global_load_dwordx4 v[186:189], v[232:233], off offset:512
	global_load_dwordx4 v[26:29], v[232:233], off offset:640
	global_load_dwordx4 v[190:193], v[234:235], off offset:512
	global_load_dwordx4 v[30:33], v[234:235], off offset:640
	v_bfe_u32 v236, v0, 5, 1
	v_mul_u32_u24_e32 v1, 0x48, v1
	v_lshlrev_b32_e32 v195, 3, v236
	v_add_lshl_u32 v238, v1, v194, 1
	v_add_lshl_u32 v1, v196, v195, 1
	v_add_u32_e32 v240, 0x9000, v238
	v_mov_b32_e32 v253, v227
	v_mov_b32_e32 v241, v227
	s_waitcnt vmcnt(47)
	ds_write_b128 v238, v[34:37]
	s_waitcnt vmcnt(46)
	ds_write_b128 v238, v[38:41] offset:36864
	s_waitcnt vmcnt(45)
	ds_write_b128 v238, v[42:45] offset:4608
	s_waitcnt vmcnt(44)
	ds_write_b128 v238, v[46:49] offset:41472
	s_waitcnt vmcnt(43)
	ds_write_b128 v238, v[50:53] offset:9216
	s_waitcnt vmcnt(42)
	ds_write_b128 v238, v[54:57] offset:46080
	s_waitcnt vmcnt(41)
	ds_write_b128 v238, v[58:61] offset:13824
	s_waitcnt vmcnt(40)
	ds_write_b128 v238, v[62:65] offset:50688
	s_waitcnt lgkmcnt(0)
	s_barrier
	ds_read_b128 v[34:37], v1
	v_and_b32_e32 v38, 0x5f, v0
	v_mul_u32_u24_e32 v38, 0x48, v38
	v_add_lshl_u32 v239, v195, v38, 1
	ds_read_b128 v[38:41], v239 offset:36864
	ds_read_b128 v[42:45], v1 offset:32
	ds_read_b128 v[46:49], v239 offset:36896
	ds_read_b128 v[50:53], v239 offset:41472
	ds_read_b128 v[54:57], v239 offset:41504
	s_waitcnt lgkmcnt(4)
	v_mfma_f32_32x32x16_bf16 a[48:63], v[34:37], v[38:41], 0
	v_and_b32_e32 v0, 64, v0
	s_waitcnt lgkmcnt(1)
	v_mfma_f32_32x32x16_bf16 a[32:47], v[34:37], v[50:53], 0
	ds_read_b128 v[34:37], v1 offset:4608
	ds_read_b128 v[58:61], v1 offset:4640
	s_waitcnt lgkmcnt(1)
	v_mfma_f32_32x32x16_bf16 a[16:31], v[34:37], v[38:41], 0
	v_mfma_f32_32x32x16_bf16 a[0:15], v[34:37], v[50:53], 0
	v_mfma_f32_32x32x16_bf16 a[48:63], v[42:45], v[46:49], a[48:63]
	v_mfma_f32_32x32x16_bf16 a[32:47], v[42:45], v[54:57], a[32:47]
	s_waitcnt lgkmcnt(0)
	v_mfma_f32_32x32x16_bf16 a[16:31], v[58:61], v[46:49], a[16:31]
	ds_read_b128 v[34:37], v1 offset:64
	ds_read_b128 v[38:41], v239 offset:36928
	ds_read_b128 v[42:45], v1 offset:96
	ds_read_b128 v[46:49], v239 offset:36960
	ds_read_b128 v[50:53], v239 offset:41536
	ds_read_b128 v[194:197], v239 offset:41568
	v_mfma_f32_32x32x16_bf16 a[0:15], v[58:61], v[54:57], a[0:15]
	s_waitcnt lgkmcnt(4)
	v_mfma_f32_32x32x16_bf16 a[48:63], v[34:37], v[38:41], a[48:63]
	s_waitcnt lgkmcnt(1)
	v_mfma_f32_32x32x16_bf16 a[32:47], v[34:37], v[50:53], a[32:47]
	ds_read_b128 v[34:37], v1 offset:4672
	ds_read_b128 v[198:201], v1 offset:4704
	s_waitcnt lgkmcnt(1)
	v_mfma_f32_32x32x16_bf16 a[16:31], v[34:37], v[38:41], a[16:31]
	v_mfma_f32_32x32x16_bf16 a[0:15], v[34:37], v[50:53], a[0:15]
	v_mfma_f32_32x32x16_bf16 a[48:63], v[42:45], v[46:49], a[48:63]
	v_mfma_f32_32x32x16_bf16 a[32:47], v[42:45], v[194:197], a[32:47]
	s_waitcnt lgkmcnt(0)
	v_mfma_f32_32x32x16_bf16 a[16:31], v[198:201], v[46:49], a[16:31]
	global_load_dwordx4 v[50:53], v[210:211], off offset:768
	global_load_dwordx4 v[54:57], v[214:215], off offset:768
	global_load_dwordx4 v[58:61], v[218:219], off offset:768
	global_load_dwordx4 v[62:65], v[222:223], off offset:768
	global_load_dwordx4 v[34:37], v[228:229], off offset:768
	global_load_dwordx4 v[38:41], v[230:231], off offset:768
	global_load_dwordx4 v[42:45], v[232:233], off offset:768
	global_load_dwordx4 v[46:49], v[234:235], off offset:768
	s_waitcnt vmcnt(47)
	ds_write_b128 v238, v[66:69] offset:18432
	s_waitcnt vmcnt(40)
	ds_write_b128 v238, v[94:97] offset:55296
	ds_write_b128 v238, v[70:73] offset:23040
	ds_write_b128 v238, v[74:77] offset:59904
	ds_write_b128 v238, v[78:81] offset:27648
	ds_write_b128 v238, v[82:85] offset:64512
	ds_write_b128 v238, v[86:89] offset:32256
	ds_write_b128 v240, v[90:93] offset:32256
	s_waitcnt lgkmcnt(0)
	s_barrier
	ds_read_b128 v[66:69], v1 offset:18432
	ds_read_b128 v[70:73], v239 offset:55296
	ds_read_b128 v[74:77], v1 offset:18464
	ds_read_b128 v[78:81], v239 offset:55328
	ds_read_b128 v[82:85], v239 offset:59904
	ds_read_b128 v[86:89], v239 offset:59936
	v_mfma_f32_32x32x16_bf16 a[0:15], v[198:201], v[194:197], a[0:15]
	s_waitcnt lgkmcnt(4)
	v_mfma_f32_32x32x16_bf16 a[48:63], v[66:69], v[70:73], a[48:63]
	s_waitcnt lgkmcnt(1)
	v_mfma_f32_32x32x16_bf16 a[32:47], v[66:69], v[82:85], a[32:47]
	ds_read_b128 v[66:69], v1 offset:23040
	ds_read_b128 v[90:93], v1 offset:23072
	s_waitcnt lgkmcnt(1)
	v_mfma_f32_32x32x16_bf16 a[16:31], v[66:69], v[70:73], a[16:31]
	v_mfma_f32_32x32x16_bf16 a[0:15], v[66:69], v[82:85], a[0:15]
	v_mfma_f32_32x32x16_bf16 a[48:63], v[74:77], v[78:81], a[48:63]
	v_mfma_f32_32x32x16_bf16 a[32:47], v[74:77], v[86:89], a[32:47]
	s_waitcnt lgkmcnt(0)
	v_mfma_f32_32x32x16_bf16 a[16:31], v[90:93], v[78:81], a[16:31]
	ds_read_b128 v[66:69], v1 offset:18496
	ds_read_b128 v[70:73], v239 offset:55360
	ds_read_b128 v[74:77], v1 offset:18528
	ds_read_b128 v[78:81], v239 offset:55392
	ds_read_b128 v[82:85], v239 offset:59968
	ds_read_b128 v[194:197], v239 offset:60000
	v_mfma_f32_32x32x16_bf16 a[0:15], v[90:93], v[86:89], a[0:15]
	s_waitcnt lgkmcnt(4)
	v_mfma_f32_32x32x16_bf16 a[48:63], v[66:69], v[70:73], a[48:63]
	s_waitcnt lgkmcnt(1)
	v_mfma_f32_32x32x16_bf16 a[32:47], v[66:69], v[82:85], a[32:47]
	ds_read_b128 v[66:69], v1 offset:23104
	ds_read_b128 v[198:201], v1 offset:23136
	s_waitcnt lgkmcnt(1)
	v_mfma_f32_32x32x16_bf16 a[16:31], v[66:69], v[70:73], a[16:31]
	v_mfma_f32_32x32x16_bf16 a[0:15], v[66:69], v[82:85], a[0:15]
	v_mfma_f32_32x32x16_bf16 a[48:63], v[74:77], v[78:81], a[48:63]
	v_mfma_f32_32x32x16_bf16 a[32:47], v[74:77], v[194:197], a[32:47]
	s_waitcnt lgkmcnt(0)
	v_mfma_f32_32x32x16_bf16 a[16:31], v[198:201], v[78:81], a[16:31]
	global_load_dwordx4 v[82:85], v[210:211], off offset:896
	global_load_dwordx4 v[86:89], v[214:215], off offset:896
	global_load_dwordx4 v[90:93], v[218:219], off offset:896
	global_load_dwordx4 v[94:97], v[222:223], off offset:896
	global_load_dwordx4 v[66:69], v[228:229], off offset:896
	global_load_dwordx4 v[70:73], v[230:231], off offset:896
	global_load_dwordx4 v[74:77], v[232:233], off offset:896
	global_load_dwordx4 v[78:81], v[234:235], off offset:896
	s_waitcnt vmcnt(46)
	ds_write_b128 v238, v[102:105]
	ds_write_b128 v238, v[98:101] offset:36864
	s_waitcnt vmcnt(44)
	ds_write_b128 v238, v[106:109] offset:4608
	s_waitcnt vmcnt(42)
	ds_write_b128 v238, v[110:113] offset:41472
	s_waitcnt vmcnt(40)
	ds_write_b128 v238, v[114:117] offset:9216
	s_waitcnt vmcnt(38)
	ds_write_b128 v238, v[118:121] offset:46080
	s_waitcnt vmcnt(36)
	ds_write_b128 v238, v[122:125] offset:13824
	s_waitcnt vmcnt(34)
	ds_write_b128 v238, v[126:129] offset:50688
	s_waitcnt lgkmcnt(0)
	s_barrier
	ds_read_b128 v[98:101], v1
	ds_read_b128 v[102:105], v239 offset:36864
	ds_read_b128 v[106:109], v1 offset:32
	ds_read_b128 v[110:113], v239 offset:36896
	ds_read_b128 v[114:117], v239 offset:41472
	ds_read_b128 v[118:121], v239 offset:41504
	v_mfma_f32_32x32x16_bf16 a[0:15], v[198:201], v[194:197], a[0:15]
	s_waitcnt lgkmcnt(4)
	v_mfma_f32_32x32x16_bf16 a[48:63], v[98:101], v[102:105], a[48:63]
	s_waitcnt lgkmcnt(1)
	v_mfma_f32_32x32x16_bf16 a[32:47], v[98:101], v[114:117], a[32:47]
	ds_read_b128 v[98:101], v1 offset:4608
	ds_read_b128 v[122:125], v1 offset:4640
	s_waitcnt lgkmcnt(1)
	v_mfma_f32_32x32x16_bf16 a[16:31], v[98:101], v[102:105], a[16:31]
	v_mfma_f32_32x32x16_bf16 a[0:15], v[98:101], v[114:117], a[0:15]
	v_mfma_f32_32x32x16_bf16 a[48:63], v[106:109], v[110:113], a[48:63]
	v_mfma_f32_32x32x16_bf16 a[32:47], v[106:109], v[118:121], a[32:47]
	s_waitcnt lgkmcnt(0)
	v_mfma_f32_32x32x16_bf16 a[16:31], v[122:125], v[110:113], a[16:31]
	ds_read_b128 v[98:101], v1 offset:64
	ds_read_b128 v[102:105], v239 offset:36928
	ds_read_b128 v[106:109], v1 offset:96
	ds_read_b128 v[110:113], v239 offset:36960
	ds_read_b128 v[114:117], v239 offset:41536
	ds_read_b128 v[194:197], v239 offset:41568
	v_mfma_f32_32x32x16_bf16 a[0:15], v[122:125], v[118:121], a[0:15]
	s_waitcnt lgkmcnt(4)
	v_mfma_f32_32x32x16_bf16 a[48:63], v[98:101], v[102:105], a[48:63]
	s_waitcnt lgkmcnt(1)
	v_mfma_f32_32x32x16_bf16 a[32:47], v[98:101], v[114:117], a[32:47]
	ds_read_b128 v[98:101], v1 offset:4672
	ds_read_b128 v[198:201], v1 offset:4704
	s_waitcnt lgkmcnt(1)
	v_mfma_f32_32x32x16_bf16 a[16:31], v[98:101], v[102:105], a[16:31]
	v_mfma_f32_32x32x16_bf16 a[0:15], v[98:101], v[114:117], a[0:15]
	v_mfma_f32_32x32x16_bf16 a[48:63], v[106:109], v[110:113], a[48:63]
	v_mfma_f32_32x32x16_bf16 a[32:47], v[106:109], v[194:197], a[32:47]
	s_waitcnt lgkmcnt(0)
	v_mfma_f32_32x32x16_bf16 a[16:31], v[198:201], v[110:113], a[16:31]
	global_load_dwordx4 v[114:117], v[210:211], off offset:1024
	global_load_dwordx4 v[118:121], v[214:215], off offset:1024
	global_load_dwordx4 v[122:125], v[218:219], off offset:1024
	global_load_dwordx4 v[126:129], v[222:223], off offset:1024
	global_load_dwordx4 v[98:101], v[228:229], off offset:1024
	global_load_dwordx4 v[102:105], v[230:231], off offset:1024
	global_load_dwordx4 v[106:109], v[232:233], off offset:1024
	global_load_dwordx4 v[110:113], v[234:235], off offset:1024
	ds_write_b128 v238, v[130:133] offset:18432
	s_waitcnt vmcnt(40)
	ds_write_b128 v238, v[174:177] offset:55296
	ds_write_b128 v238, v[134:137] offset:23040
	ds_write_b128 v238, v[138:141] offset:59904
	ds_write_b128 v238, v[142:145] offset:27648
	ds_write_b128 v238, v[146:149] offset:64512
	ds_write_b128 v238, v[150:153] offset:32256
	ds_write_b128 v240, v[170:173] offset:32256
	s_waitcnt lgkmcnt(0)
	s_barrier
	ds_read_b128 v[130:133], v1 offset:18432
	ds_read_b128 v[134:137], v239 offset:55296
	ds_read_b128 v[138:141], v1 offset:18464
	ds_read_b128 v[142:145], v239 offset:55328
	ds_read_b128 v[146:149], v239 offset:59904
	ds_read_b128 v[150:153], v239 offset:59936
	v_mfma_f32_32x32x16_bf16 a[0:15], v[198:201], v[194:197], a[0:15]
	s_waitcnt lgkmcnt(4)
	v_mfma_f32_32x32x16_bf16 a[48:63], v[130:133], v[134:137], a[48:63]
	s_waitcnt lgkmcnt(1)
	v_mfma_f32_32x32x16_bf16 a[32:47], v[130:133], v[146:149], a[32:47]
	ds_read_b128 v[130:133], v1 offset:23040
	ds_read_b128 v[170:173], v1 offset:23072
	s_waitcnt lgkmcnt(1)
	v_mfma_f32_32x32x16_bf16 a[16:31], v[130:133], v[134:137], a[16:31]
	v_mfma_f32_32x32x16_bf16 a[0:15], v[130:133], v[146:149], a[0:15]
	v_mfma_f32_32x32x16_bf16 a[48:63], v[138:141], v[142:145], a[48:63]
	v_mfma_f32_32x32x16_bf16 a[32:47], v[138:141], v[150:153], a[32:47]
	s_waitcnt lgkmcnt(0)
	v_mfma_f32_32x32x16_bf16 a[16:31], v[170:173], v[142:145], a[16:31]
	ds_read_b128 v[130:133], v1 offset:18496
	ds_read_b128 v[134:137], v239 offset:55360
	ds_read_b128 v[138:141], v1 offset:18528
	ds_read_b128 v[142:145], v239 offset:55392
	ds_read_b128 v[146:149], v239 offset:59968
	ds_read_b128 v[194:197], v239 offset:60000
	v_mfma_f32_32x32x16_bf16 a[0:15], v[170:173], v[150:153], a[0:15]
	s_waitcnt lgkmcnt(4)
	v_mfma_f32_32x32x16_bf16 a[48:63], v[130:133], v[134:137], a[48:63]
	s_waitcnt lgkmcnt(1)
	v_mfma_f32_32x32x16_bf16 a[32:47], v[130:133], v[146:149], a[32:47]
	ds_read_b128 v[130:133], v1 offset:23104
	ds_read_b128 v[198:201], v1 offset:23136
	s_waitcnt lgkmcnt(1)
	v_mfma_f32_32x32x16_bf16 a[16:31], v[130:133], v[134:137], a[16:31]
	v_mfma_f32_32x32x16_bf16 a[0:15], v[130:133], v[146:149], a[0:15]
	v_mfma_f32_32x32x16_bf16 a[48:63], v[138:141], v[142:145], a[48:63]
	v_mfma_f32_32x32x16_bf16 a[32:47], v[138:141], v[194:197], a[32:47]
	s_waitcnt lgkmcnt(0)
	v_mfma_f32_32x32x16_bf16 a[16:31], v[198:201], v[142:145], a[16:31]
	global_load_dwordx4 v[146:149], v[210:211], off offset:1152
	global_load_dwordx4 v[150:153], v[214:215], off offset:1152
	global_load_dwordx4 v[170:173], v[218:219], off offset:1152
	global_load_dwordx4 v[174:177], v[222:223], off offset:1152
	global_load_dwordx4 v[130:133], v[228:229], off offset:1152
	global_load_dwordx4 v[134:137], v[230:231], off offset:1152
	global_load_dwordx4 v[138:141], v[232:233], off offset:1152
	global_load_dwordx4 v[142:145], v[234:235], off offset:1152
	s_waitcnt vmcnt(46)
	ds_write_b128 v238, v[158:161]
	ds_write_b128 v238, v[154:157] offset:36864
	s_waitcnt vmcnt(43)
	ds_write_b128 v238, v[162:165] offset:4608
	s_waitcnt vmcnt(41)
	ds_write_b128 v238, v[166:169] offset:41472
	s_waitcnt vmcnt(39)
	ds_write_b128 v238, v[178:181] offset:9216
	s_waitcnt vmcnt(37)
	ds_write_b128 v238, v[182:185] offset:46080
	s_waitcnt vmcnt(35)
	ds_write_b128 v238, v[186:189] offset:13824
	s_waitcnt vmcnt(33)
	ds_write_b128 v238, v[190:193] offset:50688
	s_waitcnt lgkmcnt(0)
	s_barrier
	ds_read_b128 v[154:157], v1
	ds_read_b128 v[158:161], v239 offset:36864
	ds_read_b128 v[162:165], v1 offset:32
	ds_read_b128 v[166:169], v239 offset:36896
	ds_read_b128 v[178:181], v239 offset:41472
	ds_read_b128 v[182:185], v239 offset:41504
	v_mfma_f32_32x32x16_bf16 a[0:15], v[198:201], v[194:197], a[0:15]
	s_waitcnt lgkmcnt(4)
	v_mfma_f32_32x32x16_bf16 a[48:63], v[154:157], v[158:161], a[48:63]
	s_waitcnt lgkmcnt(1)
	v_mfma_f32_32x32x16_bf16 a[32:47], v[154:157], v[178:181], a[32:47]
	ds_read_b128 v[154:157], v1 offset:4608
	ds_read_b128 v[186:189], v1 offset:4640
	s_waitcnt lgkmcnt(1)
	v_mfma_f32_32x32x16_bf16 a[16:31], v[154:157], v[158:161], a[16:31]
	v_mfma_f32_32x32x16_bf16 a[0:15], v[154:157], v[178:181], a[0:15]
	v_mfma_f32_32x32x16_bf16 a[48:63], v[162:165], v[166:169], a[48:63]
	v_mfma_f32_32x32x16_bf16 a[32:47], v[162:165], v[182:185], a[32:47]
	s_waitcnt lgkmcnt(0)
	v_mfma_f32_32x32x16_bf16 a[16:31], v[186:189], v[166:169], a[16:31]
	ds_read_b128 v[154:157], v1 offset:64
	ds_read_b128 v[158:161], v239 offset:36928
	ds_read_b128 v[162:165], v1 offset:96
	ds_read_b128 v[166:169], v239 offset:36960
	ds_read_b128 v[178:181], v239 offset:41536
	ds_read_b128 v[242:245], v239 offset:41568
	v_mfma_f32_32x32x16_bf16 a[0:15], v[186:189], v[182:185], a[0:15]
	s_waitcnt lgkmcnt(4)
	v_mfma_f32_32x32x16_bf16 a[48:63], v[154:157], v[158:161], a[48:63]
	s_waitcnt lgkmcnt(1)
	v_mfma_f32_32x32x16_bf16 a[32:47], v[154:157], v[178:181], a[32:47]
	ds_read_b128 v[154:157], v1 offset:4672
	ds_read_b128 v[246:249], v1 offset:4704
	s_waitcnt lgkmcnt(1)
	v_mfma_f32_32x32x16_bf16 a[16:31], v[154:157], v[158:161], a[16:31]
	v_mfma_f32_32x32x16_bf16 a[0:15], v[154:157], v[178:181], a[0:15]
	global_load_dwordx4 v[194:197], v[210:211], off offset:1280
	global_load_dwordx4 v[198:201], v[214:215], off offset:1280
	global_load_dwordx4 v[202:205], v[218:219], off offset:1280
	global_load_dwordx4 v[206:209], v[222:223], off offset:1280
	global_load_dwordx4 v[178:181], v[228:229], off offset:1280
	global_load_dwordx4 v[182:185], v[230:231], off offset:1280
	global_load_dwordx4 v[186:189], v[232:233], off offset:1280
	global_load_dwordx4 v[190:193], v[234:235], off offset:1280
	ds_write_b128 v238, v[2:5] offset:18432
	ds_write_b128 v238, v[6:9] offset:55296
	ds_write_b128 v238, v[10:13] offset:23040
	ds_write_b128 v238, v[14:17] offset:59904
	ds_write_b128 v238, v[18:21] offset:27648
	ds_write_b128 v238, v[22:25] offset:64512
	ds_write_b128 v238, v[26:29] offset:32256
	s_waitcnt vmcnt(40)
	ds_write_b128 v240, v[30:33] offset:32256
	s_waitcnt lgkmcnt(0)
	s_barrier
	ds_read_b128 v[2:5], v1 offset:18432
	ds_read_b128 v[6:9], v239 offset:55296
	ds_read_b128 v[10:13], v1 offset:18464
	ds_read_b128 v[14:17], v239 offset:55328
	ds_read_b128 v[18:21], v239 offset:59904
	ds_read_b128 v[22:25], v239 offset:59936
	v_mfma_f32_32x32x16_bf16 a[48:63], v[162:165], v[166:169], a[48:63]
	v_mfma_f32_32x32x16_bf16 a[32:47], v[162:165], v[242:245], a[32:47]
	v_mfma_f32_32x32x16_bf16 a[16:31], v[246:249], v[166:169], a[16:31]
	v_mfma_f32_32x32x16_bf16 a[0:15], v[246:249], v[242:245], a[0:15]
	v_mov_b32_e32 v245, v227
	v_mov_b32_e32 v249, v227
	v_mov_b32_e32 v247, v227
	s_waitcnt lgkmcnt(4)
	v_mfma_f32_32x32x16_bf16 a[48:63], v[2:5], v[6:9], a[48:63]
	s_waitcnt lgkmcnt(1)
	v_mfma_f32_32x32x16_bf16 a[32:47], v[2:5], v[18:21], a[32:47]
	ds_read_b128 v[2:5], v1 offset:23040
	ds_read_b128 v[26:29], v1 offset:23072
	s_waitcnt lgkmcnt(1)
	v_mfma_f32_32x32x16_bf16 a[16:31], v[2:5], v[6:9], a[16:31]
	v_mfma_f32_32x32x16_bf16 a[0:15], v[2:5], v[18:21], a[0:15]
	v_mfma_f32_32x32x16_bf16 a[48:63], v[10:13], v[14:17], a[48:63]
	v_mfma_f32_32x32x16_bf16 a[32:47], v[10:13], v[22:25], a[32:47]
	s_waitcnt lgkmcnt(0)
	v_mfma_f32_32x32x16_bf16 a[16:31], v[26:29], v[14:17], a[16:31]
	ds_read_b128 v[2:5], v1 offset:18496
	ds_read_b128 v[6:9], v239 offset:55360
	ds_read_b128 v[10:13], v1 offset:18528
	ds_read_b128 v[14:17], v239 offset:55392
	v_mfma_f32_32x32x16_bf16 a[0:15], v[26:29], v[22:25], a[0:15]
	ds_read_b128 v[18:21], v239 offset:59968
	ds_read_b128 v[22:25], v239 offset:60000
	s_waitcnt lgkmcnt(4)
	v_mfma_f32_32x32x16_bf16 a[48:63], v[2:5], v[6:9], a[48:63]
	s_waitcnt lgkmcnt(1)
	v_mfma_f32_32x32x16_bf16 a[32:47], v[2:5], v[18:21], a[32:47]
	ds_read_b128 v[2:5], v1 offset:23104
	ds_read_b128 v[26:29], v1 offset:23136
	global_load_dwordx4 v[210:213], v[210:211], off offset:1408
	s_nop 0
	global_load_dwordx4 v[214:217], v[214:215], off offset:1408
	s_nop 0
	global_load_dwordx4 v[218:221], v[218:219], off offset:1408
	s_nop 0
	global_load_dwordx4 v[222:225], v[222:223], off offset:1408
	s_nop 0
	global_load_dwordx4 v[154:157], v[228:229], off offset:1408
	global_load_dwordx4 v[158:161], v[230:231], off offset:1408
	global_load_dwordx4 v[162:165], v[232:233], off offset:1408
	global_load_dwordx4 v[166:169], v[234:235], off offset:1408
	s_waitcnt vmcnt(47)
	ds_write_b128 v238, v[50:53]
	s_waitcnt vmcnt(46)
	ds_write_b128 v238, v[54:57] offset:36864
	s_waitcnt vmcnt(45)
	ds_write_b128 v238, v[58:61] offset:4608
	s_waitcnt vmcnt(44)
	ds_write_b128 v238, v[62:65] offset:41472
	s_waitcnt vmcnt(43)
	ds_write_b128 v238, v[34:37] offset:9216
	s_waitcnt vmcnt(42)
	ds_write_b128 v238, v[38:41] offset:46080
	s_waitcnt vmcnt(41)
	ds_write_b128 v238, v[42:45] offset:13824
	s_waitcnt vmcnt(40)
	ds_write_b128 v238, v[46:49] offset:50688
	s_waitcnt lgkmcnt(0)
	s_barrier
	v_mfma_f32_32x32x16_bf16 a[16:31], v[2:5], v[6:9], a[16:31]
	v_mov_b32_e32 v235, v227
	v_mov_b32_e32 v233, v227
	v_mov_b32_e32 v231, v227
	v_mov_b32_e32 v229, v227
	v_mfma_f32_32x32x16_bf16 a[0:15], v[2:5], v[18:21], a[0:15]
	v_mfma_f32_32x32x16_bf16 a[48:63], v[10:13], v[14:17], a[48:63]
	v_mfma_f32_32x32x16_bf16 a[32:47], v[10:13], v[22:25], a[32:47]
	v_mfma_f32_32x32x16_bf16 a[16:31], v[26:29], v[14:17], a[16:31]
	ds_read_b128 v[2:5], v1
	ds_read_b128 v[6:9], v239 offset:36864
	ds_read_b128 v[10:13], v1 offset:32
	ds_read_b128 v[14:17], v239 offset:36896
	v_mfma_f32_32x32x16_bf16 a[0:15], v[26:29], v[22:25], a[0:15]
	ds_read_b128 v[18:21], v239 offset:41472
	ds_read_b128 v[22:25], v239 offset:41504
	s_waitcnt lgkmcnt(4)
	v_mfma_f32_32x32x16_bf16 a[48:63], v[2:5], v[6:9], a[48:63]
	s_waitcnt lgkmcnt(1)
	v_mfma_f32_32x32x16_bf16 a[32:47], v[2:5], v[18:21], a[32:47]
	ds_read_b128 v[2:5], v1 offset:4608
	ds_read_b128 v[26:29], v1 offset:4640
	s_waitcnt lgkmcnt(1)
	v_mfma_f32_32x32x16_bf16 a[16:31], v[2:5], v[6:9], a[16:31]
	v_mfma_f32_32x32x16_bf16 a[0:15], v[2:5], v[18:21], a[0:15]
	v_or3_b32 v2, v0, s9, v226
	v_lshlrev_b32_e32 v0, 2, v236
	v_or3_b32 v226, s8, v237, v0
	v_or_b32_e32 v244, 1, v226
	v_lshlrev_b64 v[242:243], 12, v[226:227]
	v_or_b32_e32 v248, 3, v226
	v_or_b32_e32 v246, 8, v226
	v_mfma_f32_32x32x16_bf16 a[48:63], v[10:13], v[14:17], a[48:63]
	v_or_b32_e32 v236, 10, v226
	v_or_b32_e32 v232, 11, v226
	v_or_b32_e32 v234, 16, v226
	v_or_b32_e32 v230, 17, v226
	v_or_b32_e32 v228, 18, v226
	v_or_b32_e32 v0, 56, v226
	v_lshlrev_b32_e32 v252, 2, v2
	v_mfma_f32_32x32x16_bf16 a[32:47], v[10:13], v[22:25], a[32:47]
	v_mov_b32_e32 v237, v227
	s_waitcnt lgkmcnt(0)
	v_mfma_f32_32x32x16_bf16 a[16:31], v[26:29], v[14:17], a[16:31]
	ds_read_b128 v[6:9], v1 offset:64
	ds_read_b128 v[10:13], v239 offset:36928
	ds_read_b128 v[14:17], v1 offset:96
	ds_read_b128 v[18:21], v239 offset:36960
	v_mfma_f32_32x32x16_bf16 a[0:15], v[26:29], v[22:25], a[0:15]
	ds_read_b128 v[22:25], v239 offset:41536
	ds_read_b128 a[64:67], v239 offset:41568
	ds_read_b128 v[26:29], v1 offset:4672
	ds_read_b128 a[68:71], v1 offset:4704
	s_waitcnt vmcnt(39)
	ds_write_b128 v238, v[82:85] offset:18432
	s_waitcnt vmcnt(38)
	ds_write_b128 v238, v[86:89] offset:55296
	s_waitcnt vmcnt(37)
	ds_write_b128 v238, v[90:93] offset:23040
	s_waitcnt vmcnt(36)
	ds_write_b128 v238, v[94:97] offset:59904
	s_waitcnt vmcnt(35)
	ds_write_b128 v238, v[66:69] offset:27648
	s_waitcnt vmcnt(34)
	ds_write_b128 v238, v[70:73] offset:64512
	s_waitcnt vmcnt(33)
	ds_write_b128 v238, v[74:77] offset:32256
	s_waitcnt vmcnt(32)
	ds_write_b128 v240, v[78:81] offset:32256
	s_waitcnt lgkmcnt(0)
	s_barrier
	v_mfma_f32_32x32x16_bf16 a[48:63], v[6:9], v[10:13], a[48:63]
	v_mfma_f32_32x32x16_bf16 a[32:47], v[6:9], v[22:25], a[32:47]
	v_or_b32_e32 v8, 0x80, v252
	v_mfma_f32_32x32x16_bf16 a[16:31], v[26:29], v[10:13], a[16:31]
	v_mfma_f32_32x32x16_bf16 a[48:63], v[14:17], v[18:21], a[48:63]
	v_mfma_f32_32x32x16_bf16 a[32:47], v[14:17], a[64:67], a[32:47]
	v_mfma_f32_32x32x16_bf16 a[0:15], v[26:29], v[22:25], a[0:15]
	v_mfma_f32_32x32x16_bf16 a[16:31], a[68:71], v[18:21], a[16:31]
	ds_read_b128 v[18:21], v1 offset:18432
	ds_read_b128 v[26:29], v239 offset:55296
	ds_read_b128 v[30:33], v1 offset:18464
	ds_read_b128 v[34:37], v239 offset:55328
	ds_read_b128 v[14:17], v239 offset:59904
	ds_read_b128 a[72:75], v239 offset:59936
	s_waitcnt lgkmcnt(4)
	v_mfma_f32_32x32x16_bf16 a[48:63], v[18:21], v[26:29], a[48:63]
	s_waitcnt lgkmcnt(1)
	v_mfma_f32_32x32x16_bf16 a[32:47], v[18:21], v[14:17], a[32:47]
	ds_read_b128 v[22:25], v1 offset:23040
	ds_read_b128 v[18:21], v1 offset:23072
	s_waitcnt lgkmcnt(1)
	v_mfma_f32_32x32x16_bf16 a[16:31], v[22:25], v[26:29], a[16:31]
	v_mfma_f32_32x32x16_bf16 a[48:63], v[30:33], v[34:37], a[48:63]
	v_mfma_f32_32x32x16_bf16 a[32:47], v[30:33], a[72:75], a[32:47]
	ds_read_b128 v[30:33], v1 offset:18496
	ds_read_b128 v[42:45], v239 offset:55360
	ds_read_b128 v[46:49], v1 offset:18528
	ds_read_b128 v[50:53], v239 offset:55392
	s_waitcnt lgkmcnt(4)
	v_mfma_f32_32x32x16_bf16 a[16:31], v[18:21], v[34:37], a[16:31]
	ds_read_b128 v[34:37], v239 offset:59968
	ds_read_b128 v[26:29], v239 offset:60000
	s_waitcnt lgkmcnt(4)
	v_mfma_f32_32x32x16_bf16 a[48:63], v[30:33], v[42:45], a[48:63]
	s_waitcnt lgkmcnt(1)
	v_mfma_f32_32x32x16_bf16 a[32:47], v[30:33], v[34:37], a[32:47]
	ds_read_b128 v[38:41], v1 offset:23104
	ds_read_b128 v[30:33], v1 offset:23136
	s_waitcnt vmcnt(31)
	ds_write_b128 v238, v[114:117]
	s_waitcnt vmcnt(30)
	ds_write_b128 v238, v[118:121] offset:36864
	s_waitcnt vmcnt(29)
	ds_write_b128 v238, v[122:125] offset:4608
	s_waitcnt vmcnt(28)
	ds_write_b128 v238, v[126:129] offset:41472
	s_waitcnt vmcnt(27)
	ds_write_b128 v238, v[98:101] offset:9216
	s_waitcnt vmcnt(26)
	ds_write_b128 v238, v[102:105] offset:46080
	s_waitcnt vmcnt(25)
	ds_write_b128 v238, v[106:109] offset:13824
	s_waitcnt vmcnt(24)
	ds_write_b128 v238, v[110:113] offset:50688
	s_waitcnt lgkmcnt(0)
	s_barrier
	v_mfma_f32_32x32x16_bf16 a[16:31], v[38:41], v[42:45], a[16:31]
	v_mfma_f32_32x32x16_bf16 a[48:63], v[46:49], v[50:53], a[48:63]
	v_mfma_f32_32x32x16_bf16 a[32:47], v[46:49], v[26:29], a[32:47]
	v_mfma_f32_32x32x16_bf16 a[16:31], v[30:33], v[50:53], a[16:31]
	ds_read_b128 v[50:53], v1
	ds_read_b128 v[58:61], v239 offset:36864
	ds_read_b128 v[62:65], v1 offset:32
	ds_read_b128 v[66:69], v239 offset:36896
	ds_read_b128 v[46:49], v239 offset:41472
	ds_read_b128 v[42:45], v239 offset:41504
	s_waitcnt lgkmcnt(4)
	v_mfma_f32_32x32x16_bf16 a[48:63], v[50:53], v[58:61], a[48:63]
	s_waitcnt lgkmcnt(1)
	v_mfma_f32_32x32x16_bf16 a[32:47], v[50:53], v[46:49], a[32:47]
	ds_read_b128 v[54:57], v1 offset:4608
	ds_read_b128 v[50:53], v1 offset:4640
	s_waitcnt lgkmcnt(1)
	v_mfma_f32_32x32x16_bf16 a[16:31], v[54:57], v[58:61], a[16:31]
	v_mfma_f32_32x32x16_bf16 a[48:63], v[62:65], v[66:69], a[48:63]
	v_mfma_f32_32x32x16_bf16 a[32:47], v[62:65], v[42:45], a[32:47]
	ds_read_b128 v[62:65], v1 offset:64
	ds_read_b128 v[74:77], v239 offset:36928
	ds_read_b128 v[78:81], v1 offset:96
	ds_read_b128 v[82:85], v239 offset:36960
	s_waitcnt lgkmcnt(4)
	v_mfma_f32_32x32x16_bf16 a[16:31], v[50:53], v[66:69], a[16:31]
	ds_read_b128 v[66:69], v239 offset:41536
	ds_read_b128 v[58:61], v239 offset:41568
	s_waitcnt lgkmcnt(4)
	v_mfma_f32_32x32x16_bf16 a[48:63], v[62:65], v[74:77], a[48:63]
	s_waitcnt lgkmcnt(1)
	v_mfma_f32_32x32x16_bf16 a[32:47], v[62:65], v[66:69], a[32:47]
	ds_read_b128 v[70:73], v1 offset:4672
	ds_read_b128 v[62:65], v1 offset:4704
	s_waitcnt vmcnt(23)
	ds_write_b128 v238, v[146:149] offset:18432
	s_waitcnt vmcnt(22)
	ds_write_b128 v238, v[150:153] offset:55296
	s_waitcnt vmcnt(21)
	ds_write_b128 v238, v[170:173] offset:23040
	s_waitcnt vmcnt(20)
	ds_write_b128 v238, v[174:177] offset:59904
	s_waitcnt vmcnt(19)
	ds_write_b128 v238, v[130:133] offset:27648
	s_waitcnt vmcnt(18)
	ds_write_b128 v238, v[134:137] offset:64512
	s_waitcnt vmcnt(17)
	ds_write_b128 v238, v[138:141] offset:32256
	s_waitcnt vmcnt(16)
	ds_write_b128 v240, v[142:145] offset:32256
	s_waitcnt lgkmcnt(0)
	s_barrier
	v_mfma_f32_32x32x16_bf16 a[16:31], v[70:73], v[74:77], a[16:31]
	v_mfma_f32_32x32x16_bf16 a[48:63], v[78:81], v[82:85], a[48:63]
	v_mfma_f32_32x32x16_bf16 a[32:47], v[78:81], v[58:61], a[32:47]
	v_mfma_f32_32x32x16_bf16 a[16:31], v[62:65], v[82:85], a[16:31]
	ds_read_b128 v[82:85], v1 offset:18432
	ds_read_b128 v[90:93], v239 offset:55296
	ds_read_b128 v[94:97], v1 offset:18464
	ds_read_b128 v[98:101], v239 offset:55328
	ds_read_b128 v[78:81], v239 offset:59904
	ds_read_b128 v[74:77], v239 offset:59936
	s_waitcnt lgkmcnt(4)
	v_mfma_f32_32x32x16_bf16 a[48:63], v[82:85], v[90:93], a[48:63]
	s_waitcnt lgkmcnt(1)
	v_mfma_f32_32x32x16_bf16 a[32:47], v[82:85], v[78:81], a[32:47]
	ds_read_b128 v[86:89], v1 offset:23040
	ds_read_b128 v[82:85], v1 offset:23072
	s_waitcnt lgkmcnt(1)
	v_mfma_f32_32x32x16_bf16 a[16:31], v[86:89], v[90:93], a[16:31]
	v_mfma_f32_32x32x16_bf16 a[48:63], v[94:97], v[98:101], a[48:63]
	v_mfma_f32_32x32x16_bf16 a[32:47], v[94:97], v[74:77], a[32:47]
	ds_read_b128 v[94:97], v1 offset:18496
	ds_read_b128 v[174:177], v239 offset:55360
	ds_read_b128 v[106:109], v1 offset:18528
	ds_read_b128 v[170:173], v239 offset:55392
	s_waitcnt lgkmcnt(4)
	v_mfma_f32_32x32x16_bf16 a[16:31], v[82:85], v[98:101], a[16:31]
	ds_read_b128 v[98:101], v239 offset:59968
	ds_read_b128 v[90:93], v239 offset:60000
	s_waitcnt lgkmcnt(4)
	v_mfma_f32_32x32x16_bf16 a[48:63], v[94:97], v[174:177], a[48:63]
	s_waitcnt lgkmcnt(1)
	v_mfma_f32_32x32x16_bf16 a[32:47], v[94:97], v[98:101], a[32:47]
	ds_read_b128 v[102:105], v1 offset:23104
	ds_read_b128 v[94:97], v1 offset:23136
	s_waitcnt vmcnt(15)
	ds_write_b128 v238, v[194:197]
	s_waitcnt vmcnt(14)
	ds_write_b128 v238, v[198:201] offset:36864
	s_waitcnt vmcnt(13)
	ds_write_b128 v238, v[202:205] offset:4608
	s_waitcnt vmcnt(12)
	ds_write_b128 v238, v[206:209] offset:41472
	s_waitcnt vmcnt(11)
	ds_write_b128 v238, v[178:181] offset:9216
	s_waitcnt vmcnt(10)
	ds_write_b128 v238, v[182:185] offset:46080
	s_waitcnt vmcnt(9)
	ds_write_b128 v238, v[186:189] offset:13824
	s_waitcnt vmcnt(8)
	ds_write_b128 v238, v[190:193] offset:50688
	s_waitcnt lgkmcnt(0)
	s_barrier
	ds_read_b128 v[114:117], v1
	ds_read_b128 v[138:141], v239 offset:36864
	ds_read_b128 v[118:121], v1 offset:32
	ds_read_b128 v[142:145], v239 offset:36896
	v_mfma_f32_32x32x16_bf16 a[48:63], v[106:109], v[170:173], a[48:63]
	v_or_b32_e32 v208, 35, v226
	v_or_b32_e32 v206, 40, v226
	v_or_b32_e32 v204, 42, v226
	v_or_b32_e32 v202, 43, v226
	v_mov_b32_e32 v207, v227
	v_mov_b32_e32 v205, v227
	v_mov_b32_e32 v209, v227
	v_mfma_f32_32x32x16_bf16 a[32:47], v[106:109], v[90:93], a[32:47]
	ds_read_b128 v[110:113], v239 offset:41472
	ds_read_b128 v[106:109], v239 offset:41504
	ds_read_b128 v[122:125], v1 offset:64
	ds_read_b128 v[150:153], v239 offset:36928
	ds_read_b128 v[178:181], v1 offset:96
	ds_read_b128 v[146:149], v239 offset:36960
	v_mov_b32_e32 v203, v227
	s_waitcnt lgkmcnt(8)
	v_mfma_f32_32x32x16_bf16 a[48:63], v[114:117], v[138:141], a[48:63]
	s_waitcnt lgkmcnt(5)
	v_mfma_f32_32x32x16_bf16 a[32:47], v[114:117], v[110:113], a[32:47]
	v_mfma_f32_32x32x16_bf16 a[48:63], v[118:121], v[142:145], a[48:63]
	s_waitcnt lgkmcnt(4)
	v_mfma_f32_32x32x16_bf16 a[32:47], v[118:121], v[106:109], a[32:47]
	ds_read_b128 v[118:121], v239 offset:41536
	ds_read_b128 v[114:117], v239 offset:41568
	s_waitcnt lgkmcnt(4)
	v_mfma_f32_32x32x16_bf16 a[48:63], v[122:125], v[150:153], a[48:63]
	s_waitcnt lgkmcnt(1)
	v_mfma_f32_32x32x16_bf16 a[32:47], v[122:125], v[118:121], a[32:47]
	ds_read_b128 v[134:137], v1 offset:4608
	ds_read_b128 v[130:133], v1 offset:4640
	ds_read_b128 v[126:129], v1 offset:4672
	ds_read_b128 v[122:125], v1 offset:4704
	s_waitcnt vmcnt(7)
	ds_write_b128 v238, v[210:213] offset:18432
	s_waitcnt vmcnt(6)
	ds_write_b128 v238, v[214:217] offset:55296
	s_waitcnt vmcnt(5)
	ds_write_b128 v238, v[218:221] offset:23040
	s_waitcnt vmcnt(4)
	ds_write_b128 v238, v[222:225] offset:59904
	s_waitcnt vmcnt(3)
	ds_write_b128 v238, v[154:157] offset:27648
	s_waitcnt vmcnt(2)
	ds_write_b128 v238, v[158:161] offset:64512
	s_waitcnt vmcnt(1)
	ds_write_b128 v238, v[162:165] offset:32256
	s_waitcnt vmcnt(0)
	ds_write_b128 v240, v[166:169] offset:32256
	s_waitcnt lgkmcnt(0)
	s_barrier
	v_lshl_add_u64 v[216:217], v[226:227], 2, s[0:1]
	v_mfma_f32_32x32x16_bf16 a[48:63], v[178:181], v[146:149], a[48:63]
	v_or_b32_e32 v238, 2, v226
	v_or_b32_e32 v240, 9, v226
	v_or_b32_e32 v224, 19, v226
	v_or_b32_e32 v222, 24, v226
	v_or_b32_e32 v220, 25, v226
	v_or_b32_e32 v218, 26, v226
	v_or_b32_e32 v214, 27, v226
	v_mfma_f32_32x32x16_bf16 a[32:47], v[178:181], v[114:117], a[32:47]
	ds_read_b128 v[162:165], v1 offset:18432
	ds_read_b128 v[178:181], v239 offset:55296
	ds_read_b128 v[166:169], v1 offset:18464
	ds_read_b128 v[182:185], v239 offset:55328
	ds_read_b128 v[158:161], v239 offset:59904
	ds_read_b128 v[154:157], v239 offset:59936
	ds_read_b128 v[194:197], v1 offset:18496
	ds_read_b128 v[190:193], v239 offset:55360
	ds_read_b128 v[198:201], v1 offset:18528
	ds_read_b128 v[186:189], v239 offset:55392
	v_or_b32_e32 v212, 33, v226
	v_or_b32_e32 v210, 34, v226
	v_mov_b32_e32 v225, v227
	v_mov_b32_e32 v223, v227
	s_waitcnt lgkmcnt(8)
	v_mfma_f32_32x32x16_bf16 a[48:63], v[162:165], v[178:181], a[48:63]
	v_mov_b32_e32 v221, v227
	v_mov_b32_e32 v215, v227
	v_mov_b32_e32 v219, v227
	v_mov_b32_e32 v213, v227
	v_mov_b32_e32 v211, v227
	s_waitcnt lgkmcnt(5)
	v_mfma_f32_32x32x16_bf16 a[32:47], v[162:165], v[158:161], a[32:47]
	v_mfma_f32_32x32x16_bf16 a[48:63], v[166:169], v[182:185], a[48:63]
	s_waitcnt lgkmcnt(4)
	v_mfma_f32_32x32x16_bf16 a[32:47], v[166:169], v[154:157], a[32:47]
	ds_read_b128 v[166:169], v239 offset:59968
	ds_read_b128 v[162:165], v239 offset:60000
	v_mov_b32_e32 v239, v227
	global_load_dword v251, v252, s[2:3]
	v_lshl_add_u64 v[4:5], v[238:239], 2, s[0:1]
	s_waitcnt lgkmcnt(4)
	v_mfma_f32_32x32x16_bf16 a[48:63], v[194:197], v[190:193], a[48:63]
	s_waitcnt lgkmcnt(1)
	v_mfma_f32_32x32x16_bf16 a[32:47], v[194:197], v[166:169], a[32:47]
	v_or_b32_e32 v196, 41, v226
	v_or_b32_e32 v194, 48, v226
	v_mov_b32_e32 v195, v227
	v_mov_b32_e32 v197, v227
	v_mfma_f32_32x32x16_bf16 a[16:31], v[102:105], v[174:177], a[16:31]
	v_or_b32_e32 v174, 50, v226
	v_or_b32_e32 v176, 51, v226
	v_mov_b32_e32 v177, v227
	v_mfma_f32_32x32x16_bf16 a[48:63], v[198:201], v[186:189], a[48:63]
	s_waitcnt lgkmcnt(0)
	v_mfma_f32_32x32x16_bf16 a[32:47], v[198:201], v[162:165], a[32:47]
	v_or_b32_e32 v200, 32, v226
	v_or_b32_e32 v198, 49, v226
	v_mov_b32_e32 v201, v227
	v_mov_b32_e32 v199, v227
	s_nop 5
	v_accvgpr_read_b32 v3, a48
	v_mfma_f32_32x32x16_bf16 a[16:31], v[94:97], v[170:173], a[16:31]
	v_or_b32_e32 v172, 57, v226
	v_or_b32_e32 v170, 58, v226
	v_or_b32_e32 v226, 59, v226
	v_lshl_add_u64 v[254:255], v[226:227], 2, s[0:1]
	global_load_dword v250, v[254:255], off
	global_load_dword v2, v[216:217], off
	s_nop 0
	global_load_dwordx2 v[254:255], v[216:217], off
	v_lshl_add_u64 v[216:217], v[244:245], 2, s[0:1]
	global_load_dwordx2 v[6:7], v[216:217], off
	s_nop 0
	global_load_dwordx2 v[4:5], v[4:5], off
	s_nop 0
	global_load_dword v173, v252, s[2:3]
	global_load_dword v175, v8, s[2:3]
	v_lshl_add_u64 v[216:217], s[6:7], 0, v[252:253]
	v_lshl_add_u64 v[252:253], v[216:217], 0, v[242:243]
	v_accvgpr_read_b32 v9, a32
	v_accvgpr_read_b32 v13, a35
	v_accvgpr_read_b32 v171, a58
	v_mfma_f32_32x32x16_bf16 a[16:31], v[134:137], v[138:141], a[16:31]
	s_waitcnt vmcnt(1)
	v_add_f32_e32 v2, v173, v2
	v_fmac_f32_e32 v2, -2.0, v3
	v_xor_b32_e32 v2, 0x80000000, v2
	global_store_dword v[252:253], v2, off sc1
	v_lshl_add_u64 v[2:3], v[200:201], 2, s[0:1]
	global_load_dwordx2 v[242:243], v[2:3], off
	global_load_dword v12, v8, s[2:3]
	s_waitcnt vmcnt(3)
	v_add_f32_e32 v8, v175, v254
	v_fmac_f32_e32 v8, -2.0, v9
	v_xor_b32_e32 v8, 0x80000000, v8
	global_store_dword v[252:253], v8, off offset:128 sc1
	v_add_f32_e32 v8, v173, v255
	v_accvgpr_read_b32 v9, a49
	v_fmac_f32_e32 v8, -2.0, v9
	v_xor_b32_e32 v10, 0x80000000, v8
	v_lshlrev_b64 v[8:9], 12, v[244:245]
	v_lshl_add_u64 v[8:9], v[216:217], 0, v[8:9]
	global_store_dword v[8:9], v10, off sc1
	v_add_f32_e32 v6, v175, v6
	v_accvgpr_read_b32 v10, a33
	v_fmac_f32_e32 v6, -2.0, v10
	v_xor_b32_e32 v6, 0x80000000, v6
	global_store_dword v[8:9], v6, off offset:128 sc1
	v_add_f32_e32 v6, v173, v7
	v_accvgpr_read_b32 v7, a50
	v_fmac_f32_e32 v6, -2.0, v7
	v_xor_b32_e32 v8, 0x80000000, v6
	v_lshlrev_b64 v[6:7], 12, v[238:239]
	v_lshl_add_u64 v[6:7], v[216:217], 0, v[6:7]
	global_store_dword v[6:7], v8, off sc1
	v_add_f32_e32 v4, v175, v4
	v_accvgpr_read_b32 v8, a34
	v_fmac_f32_e32 v4, -2.0, v8
	v_xor_b32_e32 v4, 0x80000000, v4
	global_store_dword v[6:7], v4, off offset:128 sc1
	v_lshl_add_u64 v[6:7], v[248:249], 2, s[0:1]
	v_add_f32_e32 v4, v173, v5
	v_accvgpr_read_b32 v5, a51
	global_load_dword v10, v[6:7], off
	v_fmac_f32_e32 v4, -2.0, v5
	v_xor_b32_e32 v6, 0x80000000, v4
	v_lshlrev_b64 v[4:5], 12, v[248:249]
	v_lshl_add_u64 v[4:5], v[216:217], 0, v[4:5]
	global_store_dword v[4:5], v6, off sc1
	v_lshl_add_u64 v[6:7], v[246:247], 2, s[0:1]
	global_load_dword v11, v[6:7], off
	s_nop 0
	global_load_dwordx2 v[6:7], v[6:7], off
	v_lshl_add_u64 v[8:9], v[240:241], 2, s[0:1]
	global_load_dwordx2 v[8:9], v[8:9], off
	v_mfma_f32_32x32x16_bf16 a[16:31], v[130:133], v[142:145], a[16:31]
	v_lshl_add_u64 v[144:145], v[210:211], 2, s[0:1]
	s_waitcnt vmcnt(4)
	v_add_f32_e32 v10, v175, v10
	v_fmac_f32_e32 v10, -2.0, v13
	v_xor_b32_e32 v10, 0x80000000, v10
	global_store_dword v[4:5], v10, off offset:128 sc1
	v_accvgpr_read_b32 v5, a52
	v_mfma_f32_32x32x16_bf16 a[16:31], v[126:129], v[150:153], a[16:31]
	s_waitcnt vmcnt(3)
	v_add_f32_e32 v4, v173, v11
	v_fmac_f32_e32 v4, -2.0, v5
	v_xor_b32_e32 v10, 0x80000000, v4
	v_lshlrev_b64 v[4:5], 12, v[246:247]
	v_lshl_add_u64 v[4:5], v[216:217], 0, v[4:5]
	global_store_dword v[4:5], v10, off sc1
	s_waitcnt vmcnt(3)
	v_add_f32_e32 v6, v175, v6
	v_accvgpr_read_b32 v10, a36
	v_fmac_f32_e32 v6, -2.0, v10
	v_xor_b32_e32 v6, 0x80000000, v6
	global_store_dword v[4:5], v6, off offset:128 sc1
	v_add_f32_e32 v4, v173, v7
	v_accvgpr_read_b32 v5, a53
	v_fmac_f32_e32 v4, -2.0, v5
	v_xor_b32_e32 v6, 0x80000000, v4
	v_lshlrev_b64 v[4:5], 12, v[240:241]
	v_lshl_add_u64 v[4:5], v[216:217], 0, v[4:5]
	global_store_dword v[4:5], v6, off sc1
	s_waitcnt vmcnt(4)
	v_add_f32_e32 v6, v175, v8
	v_accvgpr_read_b32 v7, a37
	v_fmac_f32_e32 v6, -2.0, v7
	v_xor_b32_e32 v6, 0x80000000, v6
	global_store_dword v[4:5], v6, off offset:128 sc1
	v_lshl_add_u64 v[4:5], v[234:235], 2, s[0:1]
	v_lshl_add_u64 v[6:7], v[232:233], 2, s[0:1]
	global_load_dwordx2 v[238:239], v[4:5], off
	global_load_dword v10, v[6:7], off
	v_add_f32_e32 v6, v173, v9
	v_accvgpr_read_b32 v7, a54
	v_fmac_f32_e32 v6, -2.0, v7
	v_xor_b32_e32 v8, 0x80000000, v6
	v_lshlrev_b64 v[6:7], 12, v[236:237]
	v_lshl_add_u64 v[6:7], v[216:217], 0, v[6:7]
	global_store_dword v[6:7], v8, off sc1
	v_lshl_add_u64 v[8:9], v[236:237], 2, s[0:1]
	global_load_dwordx2 v[8:9], v[8:9], off
	v_accvgpr_read_b32 v11, a38
	v_mfma_f32_32x32x16_bf16 a[16:31], v[122:125], v[146:149], a[16:31]
	s_waitcnt vmcnt(2)
	v_add_f32_e32 v10, v175, v10
	v_mfma_f32_32x32x16_bf16 a[0:15], a[68:71], a[64:67], a[0:15]
	s_waitcnt vmcnt(0)
	v_add_f32_e32 v8, v175, v8
	v_fmac_f32_e32 v8, -2.0, v11
	v_xor_b32_e32 v8, 0x80000000, v8
	global_store_dword v[6:7], v8, off offset:128 sc1
	global_load_dword v6, v[4:5], off
	s_nop 0
	global_load_dword v11, v[2:3], off
	v_add_f32_e32 v4, v173, v9
	v_accvgpr_read_b32 v2, a55
	v_fmac_f32_e32 v4, -2.0, v2
	v_xor_b32_e32 v7, 0x80000000, v4
	v_lshlrev_b64 v[4:5], 12, v[232:233]
	v_lshl_add_u64 v[4:5], v[216:217], 0, v[4:5]
	v_lshl_add_u64 v[2:3], v[230:231], 2, s[0:1]
	global_store_dword v[4:5], v7, off sc1
	v_accvgpr_read_b32 v7, a56
	global_load_dwordx2 v[2:3], v[2:3], off
	v_accvgpr_read_b32 v9, a57
	v_lshl_add_u64 v[232:233], v[214:215], 2, s[0:1]
	v_mfma_f32_32x32x16_bf16 a[0:15], v[22:25], v[14:17], a[0:15]
	v_lshl_add_u64 v[14:15], v[194:195], 2, s[0:1]
	v_lshl_add_u64 v[16:17], v[198:199], 2, s[0:1]
	v_lshlrev_b64 v[22:23], 12, v[208:209]
	v_lshl_add_u64 v[22:23], v[216:217], 0, v[22:23]
	s_waitcnt vmcnt(3)
	v_add_f32_e32 v6, v173, v6
	v_fmac_f32_e32 v6, -2.0, v7
	v_xor_b32_e32 v8, 0x80000000, v6
	v_lshlrev_b64 v[6:7], 12, v[234:235]
	v_lshl_add_u64 v[6:7], v[216:217], 0, v[6:7]
	global_store_dword v[6:7], v8, off sc1
	v_add_f32_e32 v8, v173, v239
	v_fmac_f32_e32 v8, -2.0, v9
	v_xor_b32_e32 v13, 0x80000000, v8
	v_lshlrev_b64 v[8:9], 12, v[230:231]
	v_lshl_add_u64 v[230:231], v[228:229], 2, s[0:1]
	global_load_dwordx2 v[230:231], v[230:231], off
	v_lshl_add_u64 v[8:9], v[216:217], 0, v[8:9]
	global_store_dword v[8:9], v13, off sc1
	v_accvgpr_read_b32 v13, a39
	v_fmac_f32_e32 v10, -2.0, v13
	v_xor_b32_e32 v10, 0x80000000, v10
	global_store_dword v[4:5], v10, off offset:128 sc1
	v_lshl_add_u64 v[4:5], v[224:225], 2, s[0:1]
	global_load_dword v10, v[4:5], off
	v_lshl_add_u64 v[4:5], v[222:223], 2, s[0:1]
	global_load_dword v13, v[4:5], off
	s_waitcnt vmcnt(6)
	v_add_f32_e32 v3, v173, v3
	v_fmac_f32_e32 v3, -2.0, v171
	v_lshlrev_b64 v[228:229], 12, v[228:229]
	v_xor_b32_e32 v3, 0x80000000, v3
	v_lshl_add_u64 v[228:229], v[216:217], 0, v[228:229]
	global_store_dword v[228:229], v3, off sc1
	v_add_f32_e32 v3, v175, v238
	v_accvgpr_read_b32 v171, a40
	v_fmac_f32_e32 v3, -2.0, v171
	v_xor_b32_e32 v3, 0x80000000, v3
	global_store_dword v[6:7], v3, off offset:128 sc1
	v_accvgpr_read_b32 v6, a59
	v_lshlrev_b64 v[224:225], 12, v[224:225]
	v_lshl_add_u64 v[224:225], v[216:217], 0, v[224:225]
	v_lshlrev_b64 v[222:223], 12, v[222:223]
	v_lshl_add_u64 v[222:223], v[216:217], 0, v[222:223]
	v_add_f32_e32 v2, v175, v2
	v_mov_b32_e32 v171, v227
	v_mfma_f32_32x32x16_bf16 a[0:15], v[18:21], a[72:75], a[0:15]
	s_waitcnt vmcnt(6)
	v_add_f32_e32 v3, v173, v231
	v_fmac_f32_e32 v3, -2.0, v6
	v_lshl_add_u64 v[6:7], v[220:221], 2, s[0:1]
	global_load_dwordx2 v[6:7], v[6:7], off
	v_xor_b32_e32 v3, 0x80000000, v3
	global_load_dwordx2 v[4:5], v[4:5], off
	v_lshlrev_b64 v[220:221], 12, v[220:221]
	global_store_dword v[224:225], v3, off sc1
	v_lshl_add_u64 v[234:235], v[216:217], 0, v[220:221]
	v_mfma_f32_32x32x16_bf16 a[0:15], v[38:41], v[34:37], a[0:15]
	s_waitcnt vmcnt(5)
	v_add_f32_e32 v3, v173, v13
	v_accvgpr_read_b32 v13, a60
	v_fmac_f32_e32 v3, -2.0, v13
	global_load_dword v13, v[232:233], off
	v_lshl_add_u64 v[232:233], v[218:219], 2, s[0:1]
	global_load_dwordx2 v[232:233], v[232:233], off
	v_xor_b32_e32 v3, 0x80000000, v3
	global_store_dword v[222:223], v3, off sc1
	v_mfma_f32_32x32x16_bf16 a[0:15], v[30:33], v[26:29], a[0:15]
	v_lshl_add_u64 v[28:29], v[202:203], 2, s[0:1]
	v_lshlrev_b64 v[30:31], 12, v[204:205]
	v_lshl_add_u64 v[30:31], v[216:217], 0, v[30:31]
	v_lshlrev_b64 v[32:33], 12, v[202:203]
	v_lshl_add_u64 v[32:33], v[216:217], 0, v[32:33]
	v_lshlrev_b64 v[34:35], 12, v[194:195]
	v_lshl_add_u64 v[34:35], v[216:217], 0, v[34:35]
	v_mfma_f32_32x32x16_bf16 a[0:15], v[54:57], v[46:49], a[0:15]
	v_lshlrev_b64 v[36:37], 12, v[198:199]
	v_lshl_add_u64 v[36:37], v[216:217], 0, v[36:37]
	v_lshl_add_u64 v[40:41], v[176:177], 2, s[0:1]
	s_waitcnt vmcnt(4)
	v_add_f32_e32 v3, v173, v5
	v_accvgpr_read_b32 v5, a61
	v_fmac_f32_e32 v3, -2.0, v5
	v_xor_b32_e32 v3, 0x80000000, v3
	global_store_dword v[234:235], v3, off sc1
	v_accvgpr_read_b32 v3, a41
	v_fmac_f32_e32 v2, -2.0, v3
	v_xor_b32_e32 v2, 0x80000000, v2
	global_store_dword v[8:9], v2, off offset:128 sc1
	v_add_f32_e32 v5, v173, v7
	v_accvgpr_read_b32 v2, a62
	v_fmac_f32_e32 v5, -2.0, v2
	v_add_f32_e32 v2, v175, v230
	v_accvgpr_read_b32 v3, a42
	v_fmac_f32_e32 v2, -2.0, v3
	v_xor_b32_e32 v2, 0x80000000, v2
	global_store_dword v[228:229], v2, off offset:128 sc1
	v_lshl_add_u64 v[2:3], v[170:171], 2, s[0:1]
	v_lshl_add_u64 v[8:9], v[212:213], 2, s[0:1]
	global_load_dwordx2 v[138:139], v[2:3], off
	v_xor_b32_e32 v5, 0x80000000, v5
	global_load_dwordx2 v[8:9], v[8:9], off
	v_lshlrev_b64 v[2:3], 12, v[218:219]
	v_lshl_add_u64 v[2:3], v[216:217], 0, v[2:3]
	global_store_dword v[2:3], v5, off sc1
	ds_read_b128 v[140:143], v1 offset:23040
	ds_read_b128 v[150:153], v1 offset:23072
	s_waitcnt vmcnt(7)
	v_add_f32_e32 v5, v173, v233
	v_accvgpr_read_b32 v7, a63
	global_load_dwordx2 v[148:149], v[144:145], off
	s_waitcnt lgkmcnt(1)
	v_mfma_f32_32x32x16_bf16 a[16:31], v[140:143], v[178:181], a[16:31]
	v_fmac_f32_e32 v5, -2.0, v7
	v_add_f32_e32 v7, v175, v10
	v_accvgpr_read_b32 v10, a43
	v_fmac_f32_e32 v7, -2.0, v10
	v_lshlrev_b64 v[144:145], 12, v[214:215]
	v_xor_b32_e32 v5, 0x80000000, v5
	v_xor_b32_e32 v7, 0x80000000, v7
	v_lshl_add_u64 v[214:215], v[216:217], 0, v[144:145]
	global_store_dword v[224:225], v7, off offset:128 sc1
	global_store_dword v[214:215], v5, off sc1
	v_add_f32_e32 v7, v175, v4
	v_lshl_add_u64 v[4:5], v[206:207], 2, s[0:1]
	ds_read_b128 v[144:147], v1 offset:23104
	ds_read_b128 v[218:221], v1 offset:23136
	global_load_dword v173, v[4:5], off
	s_waitcnt lgkmcnt(2)
	v_mfma_f32_32x32x16_bf16 a[16:31], v[150:153], v[182:185], a[16:31]
	v_accvgpr_read_b32 v1, a44
	v_fmac_f32_e32 v7, -2.0, v1
	v_xor_b32_e32 v1, 0x80000000, v7
	global_store_dword v[222:223], v1, off offset:128 sc1
	v_add_f32_e32 v1, v175, v6
	v_accvgpr_read_b32 v6, a45
	v_fmac_f32_e32 v1, -2.0, v6
	s_waitcnt lgkmcnt(1)
	v_mfma_f32_32x32x16_bf16 a[16:31], v[144:147], v[190:193], a[16:31]
	v_xor_b32_e32 v1, 0x80000000, v1
	global_store_dword v[234:235], v1, off offset:128 sc1
	v_add_f32_e32 v1, v175, v232
	v_accvgpr_read_b32 v6, a46
	v_fmac_f32_e32 v1, -2.0, v6
	v_xor_b32_e32 v1, 0x80000000, v1
	global_store_dword v[2:3], v1, off offset:128 sc1
	s_waitcnt lgkmcnt(0)
	v_mfma_f32_32x32x16_bf16 a[16:31], v[218:221], v[186:189], a[16:31]
	global_load_dwordx2 v[2:3], v[4:5], off
	v_add_f32_e32 v1, v175, v13
	global_load_dword v13, v[14:15], off
	v_accvgpr_read_b32 v4, a47
	v_fmac_f32_e32 v1, -2.0, v4
	v_lshl_add_u64 v[4:5], v[196:197], 2, s[0:1]
	v_xor_b32_e32 v1, 0x80000000, v1
	global_load_dwordx2 v[4:5], v[4:5], off
	v_lshlrev_b64 v[178:179], 12, v[200:201]
	global_store_dword v[214:215], v1, off offset:128 sc1
	v_add_f32_e32 v1, v251, v11
	v_lshl_add_u64 v[178:179], v[216:217], 0, v[178:179]
	v_accvgpr_read_b32 v6, a16
	v_fmac_f32_e32 v1, -2.0, v6
	v_lshl_add_u64 v[6:7], v[204:205], 2, s[0:1]
	global_load_dwordx2 v[6:7], v[6:7], off
	v_xor_b32_e32 v1, 0x80000000, v1
	global_store_dword v[178:179], v1, off sc1
	v_add_f32_e32 v1, v251, v243
	v_accvgpr_read_b32 v10, a17
	global_load_dwordx2 v[180:181], v[14:15], off
	v_fmac_f32_e32 v1, -2.0, v10
	v_lshlrev_b64 v[10:11], 12, v[212:213]
	v_xor_b32_e32 v1, 0x80000000, v1
	v_lshl_add_u64 v[10:11], v[216:217], 0, v[10:11]
	global_store_dword v[10:11], v1, off sc1
	v_lshl_add_u64 v[14:15], v[208:209], 2, s[0:1]
	global_load_dwordx2 v[16:17], v[16:17], off
	s_nop 0
	global_load_dword v182, v[14:15], off
	v_mov_b32_e32 v175, v227
	v_lshl_add_u64 v[18:19], v[174:175], 2, s[0:1]
	global_load_dwordx2 v[18:19], v[18:19], off
	v_mfma_f32_32x32x16_bf16 a[0:15], v[50:53], v[42:45], a[0:15]
	v_lshlrev_b64 v[14:15], 12, v[210:211]
	v_lshl_add_u64 v[14:15], v[216:217], 0, v[14:15]
	v_accvgpr_read_b32 v24, a20
	v_lshlrev_b64 v[38:39], 12, v[174:175]
	v_lshl_add_u64 v[38:39], v[216:217], 0, v[38:39]
	v_lshlrev_b64 v[42:43], 12, v[176:177]
	v_lshl_add_u64 v[42:43], v[216:217], 0, v[42:43]
	v_mfma_f32_32x32x16_bf16 a[0:15], v[70:73], v[66:69], a[0:15]
	s_waitcnt vmcnt(19)
	v_add_f32_e32 v1, v251, v9
	v_accvgpr_read_b32 v9, a18
	v_fmac_f32_e32 v1, -2.0, v9
	v_xor_b32_e32 v1, 0x80000000, v1
	global_store_dword v[14:15], v1, off sc1
	v_accvgpr_read_b32 v9, a19
	v_lshlrev_b64 v[44:45], 12, v[170:171]
	v_mfma_f32_32x32x16_bf16 a[0:15], v[62:65], v[58:61], a[0:15]
	s_waitcnt vmcnt(18)
	v_add_f32_e32 v1, v251, v149
	v_fmac_f32_e32 v1, -2.0, v9
	v_xor_b32_e32 v9, 0x80000000, v1
	v_mov_b32_e32 v1, v227
	v_lshl_add_u64 v[20:21], v[0:1], 2, s[0:1]
	global_load_dword v46, v[20:21], off
	v_lshlrev_b64 v[0:1], 12, v[0:1]
	v_mfma_f32_32x32x16_bf16 a[0:15], v[86:89], v[78:81], a[0:15]
	global_store_dword v[22:23], v9, off sc1
	v_lshl_add_u64 v[0:1], v[216:217], 0, v[0:1]
	v_lshl_add_u64 v[44:45], v[216:217], 0, v[44:45]
	s_waitcnt vmcnt(17)
	v_add_f32_e32 v9, v251, v173
	v_mov_b32_e32 v173, v227
	v_lshl_add_u64 v[26:27], v[172:173], 2, s[0:1]
	global_load_dwordx2 v[26:27], v[26:27], off
	v_mfma_f32_32x32x16_bf16 a[0:15], v[82:85], v[74:77], a[0:15]
	global_load_dwordx2 v[20:21], v[20:21], off
	v_fmac_f32_e32 v9, -2.0, v24
	v_lshlrev_b64 v[24:25], 12, v[206:207]
	v_xor_b32_e32 v9, 0x80000000, v9
	v_lshl_add_u64 v[24:25], v[216:217], 0, v[24:25]
	global_store_dword v[24:25], v9, off sc1
	global_load_dword v9, v[28:29], off
	v_mfma_f32_32x32x16_bf16 a[0:15], v[102:105], v[98:101], a[0:15]
	v_accvgpr_read_b32 v28, a21
	s_waitcnt vmcnt(17)
	v_add_f32_e32 v3, v251, v3
	v_fmac_f32_e32 v3, -2.0, v28
	v_mfma_f32_32x32x16_bf16 a[0:15], v[94:97], v[90:93], a[0:15]
	v_lshlrev_b64 v[28:29], 12, v[196:197]
	v_xor_b32_e32 v3, 0x80000000, v3
	v_lshl_add_u64 v[28:29], v[216:217], 0, v[28:29]
	global_store_dword v[28:29], v3, off sc1
	s_waitcnt vmcnt(16)
	v_add_f32_e32 v3, v251, v5
	v_accvgpr_read_b32 v5, a22
	v_fmac_f32_e32 v3, -2.0, v5
	v_mfma_f32_32x32x16_bf16 a[0:15], v[134:137], v[110:113], a[0:15]
	v_xor_b32_e32 v3, 0x80000000, v3
	global_store_dword v[30:31], v3, off sc1
	v_accvgpr_read_b32 v5, a23
	v_add_f32_e32 v2, v12, v2
	s_waitcnt vmcnt(15)
	v_add_f32_e32 v3, v251, v7
	v_fmac_f32_e32 v3, -2.0, v5
	v_xor_b32_e32 v3, 0x80000000, v3
	global_store_dword v[32:33], v3, off sc1
	v_add_f32_e32 v3, v251, v13
	v_accvgpr_read_b32 v5, a24
	v_fmac_f32_e32 v3, -2.0, v5
	v_xor_b32_e32 v3, 0x80000000, v3
	global_store_dword v[34:35], v3, off sc1
	s_waitcnt vmcnt(15)
	v_add_f32_e32 v3, v251, v181
	v_accvgpr_read_b32 v5, a25
	v_mfma_f32_32x32x16_bf16 a[0:15], v[130:133], v[106:109], a[0:15]
	v_fmac_f32_e32 v3, -2.0, v5
	v_xor_b32_e32 v3, 0x80000000, v3
	global_store_dword v[36:37], v3, off sc1
	s_waitcnt vmcnt(14)
	v_add_f32_e32 v3, v251, v17
	v_accvgpr_read_b32 v5, a26
	v_fmac_f32_e32 v3, -2.0, v5
	v_xor_b32_e32 v3, 0x80000000, v3
	global_store_dword v[38:39], v3, off sc1
	s_waitcnt vmcnt(13)
	v_add_f32_e32 v3, v251, v19
	v_accvgpr_read_b32 v5, a27
	v_fmac_f32_e32 v3, -2.0, v5
	v_mfma_f32_32x32x16_bf16 a[0:15], v[126:129], v[118:121], a[0:15]
	v_xor_b32_e32 v3, 0x80000000, v3
	global_store_dword v[42:43], v3, off sc1
	global_load_dword v3, v[40:41], off
	v_accvgpr_read_b32 v7, a28
	v_lshlrev_b64 v[40:41], 12, v[172:173]
	v_lshl_add_u64 v[40:41], v[216:217], 0, v[40:41]
	s_waitcnt vmcnt(13)
	v_add_f32_e32 v5, v251, v46
	v_mfma_f32_32x32x16_bf16 a[0:15], v[122:125], v[114:117], a[0:15]
	v_fmac_f32_e32 v5, -2.0, v7
	v_xor_b32_e32 v5, 0x80000000, v5
	global_store_dword v[0:1], v5, off sc1
	v_accvgpr_read_b32 v7, a29
	v_lshlrev_b64 v[46:47], 12, v[226:227]
	v_lshl_add_u64 v[46:47], v[216:217], 0, v[46:47]
	s_waitcnt vmcnt(11)
	v_add_f32_e32 v5, v251, v21
	v_mfma_f32_32x32x16_bf16 a[0:15], v[140:143], v[158:161], a[0:15]
	v_fmac_f32_e32 v5, -2.0, v7
	v_xor_b32_e32 v5, 0x80000000, v5
	global_store_dword v[40:41], v5, off sc1
	v_add_f32_e32 v5, v251, v27
	v_accvgpr_read_b32 v7, a30
	v_fmac_f32_e32 v5, -2.0, v7
	v_xor_b32_e32 v5, 0x80000000, v5
	v_mfma_f32_32x32x16_bf16 a[0:15], v[150:153], v[154:157], a[0:15]
	global_store_dword v[44:45], v5, off sc1
	v_add_f32_e32 v5, v251, v139
	v_accvgpr_read_b32 v7, a31
	v_fmac_f32_e32 v5, -2.0, v7
	v_xor_b32_e32 v5, 0x80000000, v5
	global_store_dword v[46:47], v5, off sc1
	v_add_f32_e32 v5, v12, v242
	v_mfma_f32_32x32x16_bf16 a[0:15], v[144:147], v[166:169], a[0:15]
	v_mfma_f32_32x32x16_bf16 a[0:15], v[218:221], v[162:165], a[0:15]
	s_nop 11
	v_accvgpr_read_b32 v7, a0
	v_fmac_f32_e32 v5, -2.0, v7
	v_xor_b32_e32 v5, 0x80000000, v5
	global_store_dword v[178:179], v5, off offset:128 sc1
	v_add_f32_e32 v5, v12, v8
	v_accvgpr_read_b32 v7, a1
	v_fmac_f32_e32 v5, -2.0, v7
	v_xor_b32_e32 v5, 0x80000000, v5
	global_store_dword v[10:11], v5, off offset:128 sc1
	v_add_f32_e32 v5, v12, v148
	v_accvgpr_read_b32 v7, a2
	v_fmac_f32_e32 v5, -2.0, v7
	v_xor_b32_e32 v5, 0x80000000, v5
	global_store_dword v[14:15], v5, off offset:128 sc1
	v_add_f32_e32 v5, v12, v182
	v_accvgpr_read_b32 v7, a3
	v_fmac_f32_e32 v5, -2.0, v7
	v_xor_b32_e32 v5, 0x80000000, v5
	global_store_dword v[22:23], v5, off offset:128 sc1
	v_accvgpr_read_b32 v5, a4
	v_fmac_f32_e32 v2, -2.0, v5
	v_xor_b32_e32 v2, 0x80000000, v2
	global_store_dword v[24:25], v2, off offset:128 sc1
	v_add_f32_e32 v2, v12, v4
	v_accvgpr_read_b32 v4, a5
	v_fmac_f32_e32 v2, -2.0, v4
	v_xor_b32_e32 v2, 0x80000000, v2
	global_store_dword v[28:29], v2, off offset:128 sc1
	v_add_f32_e32 v2, v12, v6
	v_accvgpr_read_b32 v4, a6
	v_fmac_f32_e32 v2, -2.0, v4
	v_xor_b32_e32 v2, 0x80000000, v2
	global_store_dword v[30:31], v2, off offset:128 sc1
	s_waitcnt vmcnt(19)
	v_add_f32_e32 v2, v12, v9
	v_accvgpr_read_b32 v4, a7
	v_fmac_f32_e32 v2, -2.0, v4
	v_xor_b32_e32 v2, 0x80000000, v2
	global_store_dword v[32:33], v2, off offset:128 sc1
	v_add_f32_e32 v2, v12, v180
	v_accvgpr_read_b32 v4, a8
	v_fmac_f32_e32 v2, -2.0, v4
	v_xor_b32_e32 v2, 0x80000000, v2
	global_store_dword v[34:35], v2, off offset:128 sc1
	v_add_f32_e32 v2, v12, v16
	v_accvgpr_read_b32 v4, a9
	v_fmac_f32_e32 v2, -2.0, v4
	v_xor_b32_e32 v2, 0x80000000, v2
	global_store_dword v[36:37], v2, off offset:128 sc1
	v_add_f32_e32 v2, v12, v18
	v_accvgpr_read_b32 v4, a10
	v_fmac_f32_e32 v2, -2.0, v4
	v_xor_b32_e32 v2, 0x80000000, v2
	global_store_dword v[38:39], v2, off offset:128 sc1
	s_waitcnt vmcnt(15)
	v_add_f32_e32 v2, v12, v3
	v_accvgpr_read_b32 v3, a11
	v_fmac_f32_e32 v2, -2.0, v3
	v_xor_b32_e32 v2, 0x80000000, v2
	global_store_dword v[42:43], v2, off offset:128 sc1
	v_add_f32_e32 v2, v12, v20
	v_accvgpr_read_b32 v3, a12
	v_fmac_f32_e32 v2, -2.0, v3
	v_xor_b32_e32 v2, 0x80000000, v2
	global_store_dword v[0:1], v2, off offset:128 sc1
	v_add_f32_e32 v0, v12, v26
	v_accvgpr_read_b32 v1, a13
	v_fmac_f32_e32 v0, -2.0, v1
	v_xor_b32_e32 v0, 0x80000000, v0
	global_store_dword v[40:41], v0, off offset:128 sc1
	v_add_f32_e32 v0, v12, v138
	v_accvgpr_read_b32 v1, a14
	v_fmac_f32_e32 v0, -2.0, v1
	v_xor_b32_e32 v0, 0x80000000, v0
	global_store_dword v[44:45], v0, off offset:128 sc1
	v_add_f32_e32 v0, v12, v250
	v_accvgpr_read_b32 v1, a15
	v_fmac_f32_e32 v0, -2.0, v1
	v_xor_b32_e32 v0, 0x80000000, v0
	global_store_dword v[46:47], v0, off offset:128 sc1
	s_endpgm
